# router phase row loop: the 8 row loads issued together, norm gain loaded once before the loop
# speedup vs baseline: 1.0176x; 1.0047x over previous
; #define GAS __attribute__((address_space(1)))
; #define LAS __attribute__((address_space(3)))
; #define LDS_WAIT() asm volatile("s_waitcnt lgkmcnt(0)" ::: "memory")
; #define tid (tid_of(wave))
; #define lane (lane_id())
; __device__ __forceinline__ void router_phase(const Ptrs& P, const float* gain, LAS unsigned char* lds, int vcu, int G, int tid, int wave, int lane) {
;     asm volatile("" : "+v"(lane), "+v"(tid));
;     LAS unsigned* lcnt = (LAS unsigned*)(lds + RING_OFF);
;     LAS unsigned* rinfo = (LAS unsigned*)(lds + RING_OFF + 256);
;     if (tid < 16) lcnt[tid] = 0u;
;     LAS f32x4* LT = (LAS f32x4*)(lds + RING_OFF + 4096);
;     for (int i = tid; i < 2 * D; i += NWAVES * 64) { const int d = i >> 1, eq = i & 1; LT[eq * D + d] = ((const GAS f32x4*)P.router)[i]; }
;     LDS_WAIT(); __syncthreads();
;     int gw = vcu * NWAVES + wave; asm volatile("" : "+s"(gw));
;     const int NGW = G * NWAVES;
;     int li = wave;
;     for (int m = gw; m < M; m += NGW, li += NWAVES) {
;         const GAS u32x2_g* xr = (const GAS u32x2_g*)(P.H + (size_t)m * D) + lane;
;     ...
;         for (int j = 0; j < 8; ++j) { const f32x4 g = ((const GAS f32x4*)gain)[lane + 64 * j];
.LBB0_1472:
	s_mov_b64 s[26:27], 0x2000
	s_or_b64 exec, exec, s[18:19]
	s_waitcnt lgkmcnt(0)
	v_readlane_b32 s22, v253, 50
	s_waitcnt lgkmcnt(0)
	s_barrier
	s_cmpk_lt_i32 s22, 0x2000
	s_cselect_b64 s[24:25], -1, 0
	s_cmpk_gt_i32 s22, 0x1fff
	v_cmp_eq_u32_e64 s[38:39], 0, v34
	v_readlane_b32 s23, v253, 51
	s_cbranch_scc1 .LBB0_1477
	v_ashrrev_i32_e32 v35, 31, v34
	v_lshl_add_u64 v[2:3], v[34:35], 4, s[20:21]
	v_lshl_add_u64 v[38:39], v[2:3], 0, s[26:27]
	s_mov_b64 s[26:27], 0x3000
	v_lshl_add_u64 v[40:41], v[2:3], 0, s[26:27]
	s_mov_b64 s[26:27], 0x3400
	s_add_u32 s18, s16, 0x48138000
	v_lshl_add_u64 v[42:43], v[2:3], 0, s[26:27]
	s_mov_b64 s[26:27], 0x3800
	s_addc_u32 s19, s17, 0
	v_lshl_add_u64 v[44:45], v[2:3], 0, s[26:27]
	s_mov_b64 s[26:27], 0x3c00
	s_ashr_i32 s23, s22, 31
	v_lshl_add_u64 v[46:47], v[2:3], 0, s[26:27]
	s_lshl_b32 s26, s22, 1
	s_lshl_b64 s[28:29], s[22:23], 12
	v_readlane_b32 s27, v253, 30
	s_add_u32 s27, s27, s14
	v_readlane_b32 s30, v253, 31
	s_addc_u32 s30, s30, s15
	s_add_u32 s28, s27, s28
	s_addc_u32 s29, s30, s29
	v_lshl_add_u64 v[48:49], v[34:35], 3, s[28:29]
	s_lshl_b64 s[28:29], s[22:23], 11
	v_readlane_b32 s23, v253, 34
	s_add_u32 s23, s23, s14
	v_readlane_b32 s27, v253, 35
	s_addc_u32 s27, s27, s15
	s_add_u32 s28, s23, s28
	v_lshl_add_u32 v37, v34, 6, 0
	s_addc_u32 s29, s27, s29
	v_add_u32_e32 v52, 0x1000, v37
	v_lshl_add_u64 v[50:51], v[34:35], 2, s[28:29]
	v_readlane_b32 s23, v253, 20
	s_mov_b32 s30, s22
	global_load_dwordx4 v[108:111], v[38:39], off
	global_load_dwordx4 v[112:115], v[38:39], off offset:1024
	global_load_dwordx4 v[116:119], v[38:39], off offset:2048
	global_load_dwordx4 v[120:123], v[38:39], off offset:3072
	global_load_dwordx4 v[124:127], v[40:41], off
	global_load_dwordx4 v[128:131], v[42:43], off
	global_load_dwordx4 v[132:135], v[44:45], off
	global_load_dwordx4 v[136:139], v[46:47], off
	s_branch .LBB0_1475

; __device__ __forceinline__ unsigned pk4_fp8(float a, float b, float c, float d) { int w = 0; w = __builtin_amdgcn_cvt_pk_fp8_f32(a, b, w, false); w = __builtin_amdgcn_cvt_pk_fp8_f32(c, d, w, true); return (unsigned)w; }
; #define GAS __attribute__((address_space(1)))
; #define LAS __attribute__((address_space(3)))
; __device__ __forceinline__ f32x4 bf4_to_f32(u32x2_g a) { return (f32x4){__uint_as_float(a.x << 16), __uint_as_float(a.x & 0xffff0000u), __uint_as_float(a.y << 16), __uint_as_float(a.y & 0xffff0000u)}; }
; #define lane (lane_id())
; __device__ __forceinline__ void router_phase(const Ptrs& P, const float* gain, LAS unsigned char* lds, int vcu, int G, int tid, int wave, int lane) {
;     ...
;     for (int m = gw; m < M; m += NGW, li += NWAVES) {
;         const GAS u32x2_g* xr = (const GAS u32x2_g*)(P.H + (size_t)m * D) + lane;
;         f32x4 v[8]; float s = 0.f;
; #pragma unroll
;         for (int j = 0; j < 8; ++j) { v[j] = bf4_to_f32(xr[64 * j]); s += (v[j].x * v[j].x + v[j].y * v[j].y) + (v[j].z * v[j].z + v[j].w * v[j].w); }
;         const float r = 1.0f / sqrtf(wave_sum(s) * (1.0f / D) + EPS);
;         float lg[8];
; #pragma unroll
;         for (int e = 0; e < 8; ++e) lg[e] = 0.f;
;         GAS unsigned* o4 = (GAS unsigned*)(P.AB8 + (size_t)m * D) + lane;
; #pragma unroll
;         for (int j = 0; j < 8; ++j) { const f32x4 g = ((const GAS f32x4*)gain)[lane + 64 * j];
;             const float f0 = v[j].x * r * g.x, f1 = v[j].y * r * g.y, f2 = v[j].z * r * g.z, f3 = v[j].w * r * g.w;
;             o4[64 * j] = pg8::pk4_fp8(f0, f1, f2, f3);
;             const LAS f32x4* rw = LT + 256 * j + 4 * lane;
;             const f32x4 a0 = rw[0], a1 = rw[D], b0 = rw[1], b1 = rw[D + 1], c0 = rw[2], c1 = rw[D + 2], d0 = rw[3], d1 = rw[D + 3];
;             lg[0] += f0 * a0.x + f1 * b0.x + f2 * c0.x + f3 * d0.x; lg[1] += f0 * a0.y + f1 * b0.y + f2 * c0.y + f3 * d0.y;
.LBB0_1475:
	global_load_dwordx2 v[90:91], v[48:49], off offset:-2048
	global_load_dwordx2 v[104:105], v[48:49], off offset:1536
	global_load_dwordx2 v[92:93], v[48:49], off offset:-1536
	global_load_dwordx2 v[94:95], v[48:49], off offset:-1024
	global_load_dwordx2 v[96:97], v[48:49], off offset:-512
	global_load_dwordx2 v[98:99], v[48:49], off
	global_load_dwordx2 v[100:101], v[48:49], off offset:512
	global_load_dwordx2 v[102:103], v[48:49], off offset:1024
	s_waitcnt vmcnt(7)
	v_and_b32_e32 v33, 0xffff0000, v90
	v_and_b32_e32 v31, 0xffff0000, v91
	v_lshlrev_b32_e32 v35, 16, v90
	v_lshlrev_b32_e32 v32, 16, v91
	v_mul_f32_e32 v2, v33, v33
	v_mul_f32_e32 v3, v31, v31
	v_fmac_f32_e32 v2, v35, v35
	v_fmac_f32_e32 v3, v32, v32
	v_add_f32_e32 v4, v2, v3
	s_waitcnt vmcnt(6)
	v_lshlrev_b32_e32 v5, 16, v104
	s_waitcnt vmcnt(5)
	v_and_b32_e32 v29, 0xffff0000, v92
	v_and_b32_e32 v27, 0xffff0000, v93
	v_lshlrev_b32_e32 v30, 16, v92
	v_lshlrev_b32_e32 v28, 16, v93
	v_mul_f32_e32 v2, v29, v29
	v_mul_f32_e32 v3, v27, v27
	v_fmac_f32_e32 v2, v30, v30
	v_fmac_f32_e32 v3, v28, v28
	v_add_f32_e32 v2, v2, v3
	v_add_f32_e32 v4, v4, v2
	s_waitcnt vmcnt(4)
	v_and_b32_e32 v25, 0xffff0000, v94
	v_and_b32_e32 v23, 0xffff0000, v95
	v_lshlrev_b32_e32 v26, 16, v94
	v_lshlrev_b32_e32 v24, 16, v95
	v_mul_f32_e32 v2, v25, v25
	v_mul_f32_e32 v3, v23, v23
	v_fmac_f32_e32 v2, v26, v26
	v_fmac_f32_e32 v3, v24, v24
	v_add_f32_e32 v2, v2, v3
	v_add_f32_e32 v4, v4, v2
	s_waitcnt vmcnt(3)
	v_and_b32_e32 v21, 0xffff0000, v96
	v_and_b32_e32 v19, 0xffff0000, v97
	v_lshlrev_b32_e32 v22, 16, v96
	v_lshlrev_b32_e32 v20, 16, v97
	v_mul_f32_e32 v2, v21, v21
	v_mul_f32_e32 v3, v19, v19
	v_fmac_f32_e32 v2, v22, v22
	v_fmac_f32_e32 v3, v20, v20
	v_add_f32_e32 v2, v2, v3
	v_add_f32_e32 v4, v4, v2
	s_waitcnt vmcnt(2)
	v_and_b32_e32 v17, 0xffff0000, v98
	v_and_b32_e32 v15, 0xffff0000, v99
	v_lshlrev_b32_e32 v18, 16, v98
	v_lshlrev_b32_e32 v16, 16, v99
	v_mul_f32_e32 v2, v17, v17
	v_mul_f32_e32 v3, v15, v15
	v_fmac_f32_e32 v2, v18, v18
	v_fmac_f32_e32 v3, v16, v16
	v_add_f32_e32 v2, v2, v3
	v_add_f32_e32 v4, v4, v2
	s_waitcnt vmcnt(1)
	v_and_b32_e32 v13, 0xffff0000, v100
	v_and_b32_e32 v11, 0xffff0000, v101
	v_lshlrev_b32_e32 v14, 16, v100
	v_lshlrev_b32_e32 v12, 16, v101
	v_mul_f32_e32 v2, v13, v13
	v_mul_f32_e32 v3, v11, v11
	v_fmac_f32_e32 v2, v14, v14
	v_fmac_f32_e32 v3, v12, v12
	v_add_f32_e32 v2, v2, v3
	v_add_f32_e32 v4, v4, v2
	s_waitcnt vmcnt(0)
	v_and_b32_e32 v9, 0xffff0000, v102
	v_and_b32_e32 v7, 0xffff0000, v103
	v_lshlrev_b32_e32 v10, 16, v102
	v_lshlrev_b32_e32 v8, 16, v103
	v_mul_f32_e32 v2, v9, v9
	v_mul_f32_e32 v3, v7, v7
	v_fmac_f32_e32 v2, v10, v10
	v_fmac_f32_e32 v3, v8, v8
	v_add_f32_e32 v2, v2, v3
	v_add_f32_e32 v6, v4, v2
	v_and_b32_e32 v4, 0xffff0000, v104
	v_and_b32_e32 v2, 0xffff0000, v105
	v_lshlrev_b32_e32 v3, 16, v105
	v_mul_f32_e32 v53, v4, v4
	v_mul_f32_e32 v54, v2, v2
	v_fmac_f32_e32 v53, v5, v5
	v_fmac_f32_e32 v54, v3, v3
	v_add_f32_e32 v53, v53, v54
	v_add_f32_e32 v6, v6, v53
	s_nop 1
	v_add_f32_dpp v6, v6, v6 quad_perm:[1,0,3,2] row_mask:0xf bank_mask:0xf bound_ctrl:1
	s_nop 1
	v_add_f32_dpp v6, v6, v6 quad_perm:[2,3,0,1] row_mask:0xf bank_mask:0xf bound_ctrl:1
	ds_swizzle_b32 v53, v6 offset:swizzle(SWAP,4)
	s_waitcnt lgkmcnt(0)
	v_add_f32_e32 v6, v6, v53
	ds_swizzle_b32 v53, v6 offset:swizzle(SWAP,8)
	s_waitcnt lgkmcnt(0)
	v_add_f32_e32 v6, v6, v53
	ds_swizzle_b32 v53, v6 offset:swizzle(SWAP,16)
	s_waitcnt lgkmcnt(0)
	v_add_f32_e32 v6, v6, v53
	v_mov_b32_e32 v53, v6
	s_nop 1
	v_permlane32_swap_b32_e32 v6, v53
	v_add_f32_e32 v6, v6, v53
	v_fmamk_f32 v6, v6, 0x3a000000, v204
	v_cmp_gt_f32_e32 vcc, s9, v6
	v_mul_f32_e32 v53, 0x4f800000, v6
	s_nop 0
	v_cndmask_b32_e32 v6, v6, v53, vcc
	v_sqrt_f32_e32 v53, v6
	s_nop 0
	v_add_u32_e32 v54, -1, v53
	v_fma_f32 v55, -v54, v53, v6
	v_cmp_ge_f32_e64 s[40:41], 0, v55
	v_add_u32_e32 v55, 1, v53
	s_nop 0
	v_cndmask_b32_e64 v54, v53, v54, s[40:41]
	v_fma_f32 v53, -v55, v53, v6
	v_cmp_lt_f32_e64 s[40:41], 0, v53
	s_nop 1
	v_cndmask_b32_e64 v53, v54, v55, s[40:41]
	v_mul_f32_e32 v54, 0x37800000, v53
	v_cndmask_b32_e32 v53, v53, v54, vcc
	v_cmp_class_f32_e32 vcc, v6, v205
	s_nop 1
	v_cndmask_b32_e32 v6, v53, v6, vcc
	v_div_scale_f32 v53, s[28:29], v6, v6, 1.0
	v_rcp_f32_e32 v54, v53
	s_nop 0
	v_fma_f32 v55, -v53, v54, 1.0
	v_fmac_f32_e32 v54, v55, v54
	v_div_scale_f32 v55, vcc, 1.0, v6, 1.0
	v_mul_f32_e32 v56, v55, v54
	v_fma_f32 v57, -v53, v56, v55
	v_fmac_f32_e32 v56, v57, v54
	v_fma_f32 v53, -v53, v56, v55
	v_div_fmas_f32 v53, v53, v54, v56
	v_div_fixup_f32 v6, v53, v6, 1.0
	v_mul_f32_e32 v35, v6, v35
	v_mul_f32_e32 v33, v6, v33
	v_mov_b32_e32 v53, v1
	v_mul_f32_e32 v32, v6, v32
	v_mul_f32_e32 v31, v6, v31
	v_mul_f32_e32 v30, v6, v30
	v_mul_f32_e32 v29, v6, v29
	v_mul_f32_e32 v28, v6, v28
	v_mul_f32_e32 v27, v6, v27
	v_mul_f32_e32 v26, v6, v26
	v_mul_f32_e32 v25, v6, v25
	v_mul_f32_e32 v24, v6, v24
	v_mul_f32_e32 v23, v6, v23
	v_mul_f32_e32 v22, v6, v22
	v_mul_f32_e32 v21, v6, v21
	v_mul_f32_e32 v20, v6, v20
	v_mul_f32_e32 v19, v6, v19
	v_mul_f32_e32 v18, v6, v18
	v_mul_f32_e32 v17, v6, v17
	v_mul_f32_e32 v16, v6, v16
	v_mul_f32_e32 v15, v6, v15
	v_mul_f32_e32 v14, v6, v14
	v_mul_f32_e32 v13, v6, v13
	v_mul_f32_e32 v12, v6, v12
	v_mul_f32_e32 v11, v6, v11
	v_mul_f32_e32 v10, v6, v10
	v_mul_f32_e32 v9, v6, v9
	v_mul_f32_e32 v8, v6, v8
	v_mul_f32_e32 v7, v6, v7
	v_mul_f32_e32 v5, v6, v5
	v_mul_f32_e32 v4, v6, v4
	v_mul_f32_e32 v2, v6, v2
	v_mul_f32_e32 v3, v6, v3
	v_mul_f32_e32 v35, v108, v35
	v_mul_f32_e32 v33, v109, v33
	v_cvt_pk_fp8_f32 v53, v35, v33
	v_mul_f32_e32 v32, v110, v32
	v_mul_f32_e32 v31, v111, v31
	v_cvt_pk_fp8_f32 v53, v32, v31 op_sel:[0,0,1]
	global_store_dword v[50:51], v53, off offset:-1024 sc0 sc1
	ds_read_b128 v[54:57], v37 offset:36864
	ds_read_b128 v[58:61], v37 offset:36880
	ds_read_b128 v[62:65], v37 offset:36896
	ds_read_b128 v[66:69], v37 offset:4096
	ds_read_b128 v[70:73], v37 offset:4112
	ds_read_b128 v[74:77], v37 offset:4128
	ds_read_b128 v[78:81], v37 offset:4144
	ds_read_b128 v[82:85], v37 offset:36912
	s_waitcnt lgkmcnt(6)
; __device__ __forceinline__ unsigned pk4_fp8(float a, float b, float c, float d) { int w = 0; w = __builtin_amdgcn_cvt_pk_fp8_f32(a, b, w, false); w = __builtin_amdgcn_cvt_pk_fp8_f32(c, d, w, true); return (unsigned)w; }
; #define GAS __attribute__((address_space(1)))
; #define LAS __attribute__((address_space(3)))
; #define lane (lane_id())
; __device__ __forceinline__ void router_phase(const Ptrs& P, const float* gain, LAS unsigned char* lds, int vcu, int G, int tid, int wave, int lane) {
;     ...
;         for (int j = 0; j < 8; ++j) { const f32x4 g = ((const GAS f32x4*)gain)[lane + 64 * j];
;             const float f0 = v[j].x * r * g.x, f1 = v[j].y * r * g.y, f2 = v[j].z * r * g.z, f3 = v[j].w * r * g.w;
;             o4[64 * j] = pg8::pk4_fp8(f0, f1, f2, f3);
;             const LAS f32x4* rw = LT + 256 * j + 4 * lane;
;             const f32x4 a0 = rw[0], a1 = rw[D], b0 = rw[1], b1 = rw[D + 1], c0 = rw[2], c1 = rw[D + 2], d0 = rw[3], d1 = rw[D + 3];
;             lg[0] += f0 * a0.x + f1 * b0.x + f2 * c0.x + f3 * d0.x; lg[1] += f0 * a0.y + f1 * b0.y + f2 * c0.y + f3 * d0.y;
;             lg[2] += f0 * a0.z + f1 * b0.z + f2 * c0.z + f3 * d0.z; lg[3] += f0 * a0.w + f1 * b0.w + f2 * c0.w + f3 * d0.w;
;             lg[4] += f0 * a1.x + f1 * b1.x + f2 * c1.x + f3 * d1.x; lg[5] += f0 * a1.y + f1 * b1.y + f2 * c1.y + f3 * d1.y;
;             lg[6] += f0 * a1.z + f1 * b1.z + f2 * c1.z + f3 * d1.z; lg[7] += f0 * a1.w + f1 * b1.w + f2 * c1.w + f3 * d1.w; }
	v_mul_f32_e32 v58, v33, v58
	s_waitcnt lgkmcnt(3)
	v_mul_f32_e32 v53, v70, v33
	v_fmac_f32_e32 v53, v66, v35
	v_mul_f32_e32 v66, v71, v33
	v_fmac_f32_e32 v66, v67, v35
	v_fmac_f32_e32 v58, v54, v35
	v_mul_f32_e32 v54, v33, v59
	s_waitcnt lgkmcnt(2)
	v_fmac_f32_e32 v66, v32, v75
	v_fmac_f32_e32 v54, v55, v35
	s_waitcnt lgkmcnt(1)
	v_fmac_f32_e32 v66, v31, v79
	v_fmac_f32_e32 v54, v32, v63
	v_add_f32_e32 v86, 0, v66
	v_mul_f32_e32 v66, v72, v33
	s_waitcnt lgkmcnt(0)
	v_fmac_f32_e32 v54, v31, v83
	v_fmac_f32_e32 v66, v68, v35
	v_add_f32_e32 v83, 0, v54
	v_mul_f32_e32 v54, v33, v60
	v_fmac_f32_e32 v66, v32, v76
	v_fmac_f32_e32 v54, v56, v35
	v_fmac_f32_e32 v66, v31, v80
	v_fmac_f32_e32 v54, v32, v64
	v_add_f32_e32 v87, 0, v66
	v_mul_f32_e32 v66, v73, v33
	v_fmac_f32_e32 v54, v31, v84
	v_mul_f32_e32 v33, v33, v61
	v_add_f32_e32 v84, 0, v54
	v_fmac_f32_e32 v33, v57, v35
	v_fmac_f32_e32 v33, v32, v65
	v_fmac_f32_e32 v66, v69, v35
	v_fmac_f32_e32 v33, v31, v85
	v_fmac_f32_e32 v53, v32, v74
	v_fmac_f32_e32 v66, v32, v77
	v_fmac_f32_e32 v58, v32, v62
	v_add_f32_e32 v32, 0, v33
	v_fmac_f32_e32 v66, v31, v81
	v_fmac_f32_e32 v58, v31, v82
	v_fmac_f32_e32 v53, v31, v78
	v_add_f32_e32 v88, 0, v66
	v_add_f32_e32 v82, 0, v58
	v_add_f32_e32 v53, 0, v53
	v_mul_f32_e32 v33, v30, v112
	v_mul_f32_e32 v35, v29, v113
	v_mul_f32_e32 v85, v28, v114
	v_mov_b32_e32 v28, v1
	v_cvt_pk_fp8_f32 v28, v33, v35
	v_mul_f32_e32 v27, v27, v115
	v_cvt_pk_fp8_f32 v28, v85, v27 op_sel:[0,0,1]
	global_store_dword v[50:51], v28, off offset:-768 sc0 sc1
	ds_read_b128 v[28:31], v37 offset:40960
	ds_read_b128 v[54:57], v37 offset:40976
	ds_read_b128 v[58:61], v37 offset:40992
	ds_read_b128 v[62:65], v37 offset:8192
	ds_read_b128 v[66:69], v37 offset:8208
	ds_read_b128 v[70:73], v37 offset:8224
	ds_read_b128 v[74:77], v37 offset:8240
	ds_read_b128 v[78:81], v37 offset:41008
	s_waitcnt lgkmcnt(6)
	v_mul_f32_e32 v54, v35, v54
	v_fmac_f32_e32 v54, v33, v28
	v_mul_f32_e32 v28, v35, v55
	v_fmac_f32_e32 v28, v33, v29
	s_waitcnt lgkmcnt(5)
	v_fmac_f32_e32 v28, v85, v59
	s_waitcnt lgkmcnt(0)
	v_fmac_f32_e32 v28, v27, v79
	v_add_f32_e32 v79, v83, v28
	v_mul_f32_e32 v28, v35, v56
	v_fmac_f32_e32 v28, v33, v30
	v_fmac_f32_e32 v28, v85, v60
	v_fmac_f32_e32 v28, v27, v80
	v_add_f32_e32 v80, v84, v28
	v_mul_f32_e32 v28, v35, v57
	v_fmac_f32_e32 v28, v33, v31
	v_fmac_f32_e32 v28, v85, v61
	v_fmac_f32_e32 v28, v27, v81
	v_add_f32_e32 v32, v32, v28
	v_mul_f32_e32 v66, v35, v66
	v_fmac_f32_e32 v66, v33, v62
	v_mul_f32_e32 v62, v35, v67
	v_fmac_f32_e32 v62, v33, v63
	v_fmac_f32_e32 v62, v85, v71
	v_fmac_f32_e32 v62, v27, v75
	v_add_f32_e32 v86, v86, v62
	v_mul_f32_e32 v62, v35, v68
	v_fmac_f32_e32 v62, v33, v64
	v_fmac_f32_e32 v62, v85, v72
	v_fmac_f32_e32 v62, v27, v76
	v_add_f32_e32 v87, v87, v62
	v_mul_f32_e32 v62, v35, v69
	v_fmac_f32_e32 v62, v33, v65
	v_fmac_f32_e32 v66, v85, v70
	v_fmac_f32_e32 v62, v85, v73
	v_fmac_f32_e32 v54, v85, v58
	v_fmac_f32_e32 v66, v27, v74
	v_fmac_f32_e32 v62, v27, v77
	v_fmac_f32_e32 v54, v27, v78
	v_add_f32_e32 v53, v53, v66
	v_add_f32_e32 v88, v88, v62
	v_add_f32_e32 v78, v82, v54
	v_mul_f32_e32 v33, v26, v116
	v_mul_f32_e32 v35, v25, v117
	v_mul_f32_e32 v81, v24, v118
	v_mov_b32_e32 v24, v1
	v_cvt_pk_fp8_f32 v24, v33, v35
	v_mul_f32_e32 v23, v23, v119
	v_cvt_pk_fp8_f32 v24, v81, v23 op_sel:[0,0,1]
	global_store_dword v[50:51], v24, off offset:-512 sc0 sc1
	ds_read_b128 v[24:27], v37 offset:45056
	ds_read_b128 v[28:31], v37 offset:45072
	ds_read_b128 v[54:57], v37 offset:45088
	ds_read_b128 v[58:61], v37 offset:12288
	ds_read_b128 v[62:65], v37 offset:12304
	ds_read_b128 v[66:69], v37 offset:12320
	ds_read_b128 v[70:73], v37 offset:12336
	ds_read_b128 v[74:77], v37 offset:45104
	s_waitcnt lgkmcnt(6)
	v_mul_f32_e32 v28, v35, v28
	v_fmac_f32_e32 v28, v33, v24
	v_mul_f32_e32 v24, v35, v29
	v_fmac_f32_e32 v24, v33, v25
	s_waitcnt lgkmcnt(5)
	v_fmac_f32_e32 v24, v81, v55
	s_waitcnt lgkmcnt(0)
	v_fmac_f32_e32 v24, v23, v75
	v_add_f32_e32 v75, v79, v24
	v_mul_f32_e32 v24, v35, v30
	v_fmac_f32_e32 v24, v33, v26
	v_fmac_f32_e32 v24, v81, v56
	v_fmac_f32_e32 v24, v23, v76
	v_add_f32_e32 v76, v80, v24
	v_mul_f32_e32 v24, v35, v31
	v_fmac_f32_e32 v24, v33, v27
	v_fmac_f32_e32 v24, v81, v57
	v_fmac_f32_e32 v24, v23, v77
	v_add_f32_e32 v32, v32, v24
	v_mul_f32_e32 v62, v35, v62
	v_fmac_f32_e32 v62, v33, v58
	v_mul_f32_e32 v58, v35, v63
	v_fmac_f32_e32 v58, v33, v59
	v_fmac_f32_e32 v58, v81, v67
	v_fmac_f32_e32 v58, v23, v71
	v_add_f32_e32 v82, v86, v58
	v_mul_f32_e32 v58, v35, v64
	v_fmac_f32_e32 v58, v33, v60
	v_fmac_f32_e32 v58, v81, v68
	v_fmac_f32_e32 v58, v23, v72
	v_add_f32_e32 v83, v87, v58
	v_mul_f32_e32 v58, v35, v65
	v_fmac_f32_e32 v58, v33, v61
	v_fmac_f32_e32 v62, v81, v66
	v_fmac_f32_e32 v58, v81, v69
	v_fmac_f32_e32 v28, v81, v54
	v_fmac_f32_e32 v62, v23, v70
	v_fmac_f32_e32 v58, v23, v73
	v_fmac_f32_e32 v28, v23, v74
	v_add_f32_e32 v53, v53, v62
	v_add_f32_e32 v84, v88, v58
	v_add_f32_e32 v74, v78, v28
	v_mul_f32_e32 v33, v22, v120
	v_mul_f32_e32 v35, v21, v121
	v_mul_f32_e32 v77, v20, v122
	v_mov_b32_e32 v20, v1
	v_cvt_pk_fp8_f32 v20, v33, v35
	v_mul_f32_e32 v19, v19, v123
	v_cvt_pk_fp8_f32 v20, v77, v19 op_sel:[0,0,1]
	global_store_dword v[50:51], v20, off offset:-256 sc0 sc1
	ds_read_b128 v[20:23], v37 offset:49152
	ds_read_b128 v[24:27], v37 offset:49168
	ds_read_b128 v[28:31], v37 offset:49184
	ds_read_b128 v[54:57], v37 offset:16384
	ds_read_b128 v[58:61], v37 offset:16400
	ds_read_b128 v[62:65], v37 offset:16416
	ds_read_b128 v[66:69], v37 offset:16432
	ds_read_b128 v[70:73], v37 offset:49200
	s_waitcnt lgkmcnt(6)
; __device__ __forceinline__ unsigned pk4_fp8(float a, float b, float c, float d) { int w = 0; w = __builtin_amdgcn_cvt_pk_fp8_f32(a, b, w, false); w = __builtin_amdgcn_cvt_pk_fp8_f32(c, d, w, true); return (unsigned)w; }
; #define GAS __attribute__((address_space(1)))
; #define LAS __attribute__((address_space(3)))
; #define lane (lane_id())
; __device__ __forceinline__ void router_phase(const Ptrs& P, const float* gain, LAS unsigned char* lds, int vcu, int G, int tid, int wave, int lane) {
;     ...
;         for (int j = 0; j < 8; ++j) { const f32x4 g = ((const GAS f32x4*)gain)[lane + 64 * j];
;             const float f0 = v[j].x * r * g.x, f1 = v[j].y * r * g.y, f2 = v[j].z * r * g.z, f3 = v[j].w * r * g.w;
;             o4[64 * j] = pg8::pk4_fp8(f0, f1, f2, f3);
;             const LAS f32x4* rw = LT + 256 * j + 4 * lane;
;             const f32x4 a0 = rw[0], a1 = rw[D], b0 = rw[1], b1 = rw[D + 1], c0 = rw[2], c1 = rw[D + 2], d0 = rw[3], d1 = rw[D + 3];
;             lg[0] += f0 * a0.x + f1 * b0.x + f2 * c0.x + f3 * d0.x; lg[1] += f0 * a0.y + f1 * b0.y + f2 * c0.y + f3 * d0.y;
;             lg[2] += f0 * a0.z + f1 * b0.z + f2 * c0.z + f3 * d0.z; lg[3] += f0 * a0.w + f1 * b0.w + f2 * c0.w + f3 * d0.w;
;             lg[4] += f0 * a1.x + f1 * b1.x + f2 * c1.x + f3 * d1.x; lg[5] += f0 * a1.y + f1 * b1.y + f2 * c1.y + f3 * d1.y;
;             lg[6] += f0 * a1.z + f1 * b1.z + f2 * c1.z + f3 * d1.z; lg[7] += f0 * a1.w + f1 * b1.w + f2 * c1.w + f3 * d1.w; }
	v_mul_f32_e32 v24, v35, v24
	v_fmac_f32_e32 v24, v33, v20
	v_mul_f32_e32 v20, v35, v25
	v_fmac_f32_e32 v20, v33, v21
	s_waitcnt lgkmcnt(5)
	v_fmac_f32_e32 v20, v77, v29
	s_waitcnt lgkmcnt(0)
	v_fmac_f32_e32 v20, v19, v71
	v_add_f32_e32 v71, v75, v20
	v_mul_f32_e32 v20, v35, v26
	v_fmac_f32_e32 v20, v33, v22
	v_fmac_f32_e32 v20, v77, v30
	v_fmac_f32_e32 v20, v19, v72
	v_add_f32_e32 v72, v76, v20
	v_mul_f32_e32 v20, v35, v27
	v_fmac_f32_e32 v20, v33, v23
	v_fmac_f32_e32 v20, v77, v31
	v_fmac_f32_e32 v20, v19, v73
	v_add_f32_e32 v32, v32, v20
	v_mul_f32_e32 v58, v35, v58
	v_fmac_f32_e32 v58, v33, v54
	v_mul_f32_e32 v54, v35, v59
	v_fmac_f32_e32 v54, v33, v55
	v_fmac_f32_e32 v54, v77, v63
	v_fmac_f32_e32 v54, v19, v67
	v_add_f32_e32 v78, v82, v54
	v_mul_f32_e32 v54, v35, v60
	v_fmac_f32_e32 v54, v33, v56
	v_fmac_f32_e32 v54, v77, v64
	v_fmac_f32_e32 v54, v19, v68
	v_add_f32_e32 v79, v83, v54
	v_mul_f32_e32 v54, v35, v61
	v_fmac_f32_e32 v54, v33, v57
	v_fmac_f32_e32 v58, v77, v62
	v_fmac_f32_e32 v54, v77, v65
	v_fmac_f32_e32 v24, v77, v28
	v_fmac_f32_e32 v58, v19, v66
	v_fmac_f32_e32 v54, v19, v69
	v_fmac_f32_e32 v24, v19, v70
	v_add_f32_e32 v53, v53, v58
	v_add_f32_e32 v80, v84, v54
	v_add_f32_e32 v70, v74, v24
	v_mul_f32_e32 v33, v18, v124
	v_mul_f32_e32 v35, v17, v125
	v_mul_f32_e32 v73, v16, v126
	v_mov_b32_e32 v16, v1
	v_cvt_pk_fp8_f32 v16, v33, v35
	v_mul_f32_e32 v15, v15, v127
	v_cvt_pk_fp8_f32 v16, v73, v15 op_sel:[0,0,1]
	global_store_dword v[50:51], v16, off sc0 sc1
	ds_read_b128 v[16:19], v37 offset:53248
	ds_read_b128 v[20:23], v37 offset:53264
	ds_read_b128 v[24:27], v37 offset:53280
	ds_read_b128 v[28:31], v37 offset:20480
	ds_read_b128 v[54:57], v37 offset:20496
	ds_read_b128 v[58:61], v37 offset:20512
	ds_read_b128 v[62:65], v37 offset:20528
	ds_read_b128 v[66:69], v37 offset:53296
	s_waitcnt lgkmcnt(6)
	v_mul_f32_e32 v20, v35, v20
	v_fmac_f32_e32 v20, v33, v16
	v_mul_f32_e32 v16, v35, v21
	v_fmac_f32_e32 v16, v33, v17
	s_waitcnt lgkmcnt(5)
	v_fmac_f32_e32 v16, v73, v25
	s_waitcnt lgkmcnt(0)
	v_fmac_f32_e32 v16, v15, v67
	v_add_f32_e32 v67, v71, v16
	v_mul_f32_e32 v16, v35, v22
	v_fmac_f32_e32 v16, v33, v18
	v_fmac_f32_e32 v16, v73, v26
	v_fmac_f32_e32 v16, v15, v68
	v_add_f32_e32 v68, v72, v16
	v_mul_f32_e32 v16, v35, v23
	v_fmac_f32_e32 v16, v33, v19
	v_fmac_f32_e32 v16, v73, v27
	v_fmac_f32_e32 v16, v15, v69
	v_add_f32_e32 v32, v32, v16
	v_mul_f32_e32 v54, v35, v54
	v_fmac_f32_e32 v54, v33, v28
	v_mul_f32_e32 v28, v35, v55
	v_fmac_f32_e32 v28, v33, v29
	v_fmac_f32_e32 v28, v73, v59
	v_fmac_f32_e32 v28, v15, v63
	v_add_f32_e32 v74, v78, v28
	v_mul_f32_e32 v28, v35, v56
	v_fmac_f32_e32 v28, v33, v30
	v_fmac_f32_e32 v28, v73, v60
	v_fmac_f32_e32 v28, v15, v64
	v_add_f32_e32 v75, v79, v28
	v_mul_f32_e32 v28, v35, v57
	v_fmac_f32_e32 v28, v33, v31
	v_fmac_f32_e32 v54, v73, v58
	v_fmac_f32_e32 v28, v73, v61
	v_fmac_f32_e32 v20, v73, v24
	v_fmac_f32_e32 v54, v15, v62
	v_fmac_f32_e32 v28, v15, v65
	v_fmac_f32_e32 v20, v15, v66
	v_add_f32_e32 v53, v53, v54
	v_add_f32_e32 v76, v80, v28
	v_add_f32_e32 v66, v70, v20
	v_mul_f32_e32 v33, v14, v128
	v_mul_f32_e32 v35, v13, v129
	v_mul_f32_e32 v69, v12, v130
	v_mov_b32_e32 v12, v1
	v_cvt_pk_fp8_f32 v12, v33, v35
	v_mul_f32_e32 v11, v11, v131
	v_cvt_pk_fp8_f32 v12, v69, v11 op_sel:[0,0,1]
	global_store_dword v[50:51], v12, off offset:256 sc0 sc1
	ds_read_b128 v[12:15], v37 offset:57344
	ds_read_b128 v[16:19], v37 offset:57360
	ds_read_b128 v[20:23], v37 offset:57376
	ds_read_b128 v[24:27], v37 offset:24576
	ds_read_b128 v[28:31], v37 offset:24592
	ds_read_b128 v[54:57], v37 offset:24608
	ds_read_b128 v[58:61], v37 offset:24624
	ds_read_b128 v[62:65], v37 offset:57392
	s_waitcnt lgkmcnt(6)
	v_mul_f32_e32 v16, v35, v16
	v_fmac_f32_e32 v16, v33, v12
	v_mul_f32_e32 v12, v35, v17
	v_fmac_f32_e32 v12, v33, v13
	s_waitcnt lgkmcnt(5)
	v_fmac_f32_e32 v12, v69, v21
	s_waitcnt lgkmcnt(0)
	v_fmac_f32_e32 v12, v11, v63
	v_add_f32_e32 v71, v67, v12
	v_mul_f32_e32 v12, v35, v18
	v_fmac_f32_e32 v12, v33, v14
	v_fmac_f32_e32 v12, v69, v22
	v_fmac_f32_e32 v12, v11, v64
	v_add_f32_e32 v68, v68, v12
	v_mul_f32_e32 v12, v35, v19
	v_fmac_f32_e32 v12, v33, v15
	v_fmac_f32_e32 v12, v69, v23
	v_fmac_f32_e32 v12, v11, v65
	v_add_f32_e32 v32, v32, v12
	v_mul_f32_e32 v28, v35, v28
	v_fmac_f32_e32 v28, v33, v24
	v_mul_f32_e32 v24, v35, v29
	v_fmac_f32_e32 v24, v33, v25
	v_fmac_f32_e32 v24, v69, v55
	v_fmac_f32_e32 v28, v69, v54
	v_fmac_f32_e32 v24, v11, v59
	v_fmac_f32_e32 v28, v11, v58
	v_add_f32_e32 v58, v74, v24
	v_mul_f32_e32 v24, v35, v30
	v_fmac_f32_e32 v24, v33, v26
	v_fmac_f32_e32 v24, v69, v56
	v_fmac_f32_e32 v24, v11, v60
	v_add_f32_e32 v59, v75, v24
	v_mul_f32_e32 v24, v35, v31
	v_fmac_f32_e32 v24, v33, v27
	v_fmac_f32_e32 v24, v69, v57
	v_fmac_f32_e32 v16, v69, v20
	v_fmac_f32_e32 v24, v11, v61
	v_fmac_f32_e32 v16, v11, v62
	v_add_f32_e32 v53, v53, v28
	v_add_f32_e32 v60, v76, v24
	v_add_f32_e32 v70, v66, v16
	v_mul_f32_e32 v33, v10, v132
	v_mul_f32_e32 v35, v9, v133
	v_mul_f32_e32 v69, v8, v134
	v_mov_b32_e32 v8, v1
	v_cvt_pk_fp8_f32 v8, v33, v35
	v_mul_f32_e32 v7, v7, v135
	v_cvt_pk_fp8_f32 v8, v69, v7 op_sel:[0,0,1]
	global_store_dword v[50:51], v8, off offset:512 sc0 sc1
	ds_read_b128 v[8:11], v37 offset:61440
	ds_read_b128 v[12:15], v37 offset:61456
	ds_read_b128 v[16:19], v37 offset:61472
	ds_read_b128 v[20:23], v37 offset:28672
	ds_read_b128 v[24:27], v37 offset:28688
	ds_read_b128 v[28:31], v37 offset:28704
	ds_read_b128 v[54:57], v37 offset:28720
	ds_read_b128 v[64:67], v37 offset:61488
	s_waitcnt lgkmcnt(6)
	v_mul_f32_e32 v12, v35, v12
	s_waitcnt lgkmcnt(3)
; __device__ __forceinline__ unsigned pk4_fp8(float a, float b, float c, float d) { int w = 0; w = __builtin_amdgcn_cvt_pk_fp8_f32(a, b, w, false); w = __builtin_amdgcn_cvt_pk_fp8_f32(c, d, w, true); return (unsigned)w; }
; #define GAS __attribute__((address_space(1)))
; #define LAS __attribute__((address_space(3)))
; #define lane (lane_id())
; __device__ __forceinline__ void router_phase(const Ptrs& P, const float* gain, LAS unsigned char* lds, int vcu, int G, int tid, int wave, int lane) {
;     ...
;         for (int j = 0; j < 8; ++j) { const f32x4 g = ((const GAS f32x4*)gain)[lane + 64 * j];
;             const float f0 = v[j].x * r * g.x, f1 = v[j].y * r * g.y, f2 = v[j].z * r * g.z, f3 = v[j].w * r * g.w;
;             o4[64 * j] = pg8::pk4_fp8(f0, f1, f2, f3);
;             const LAS f32x4* rw = LT + 256 * j + 4 * lane;
;             const f32x4 a0 = rw[0], a1 = rw[D], b0 = rw[1], b1 = rw[D + 1], c0 = rw[2], c1 = rw[D + 2], d0 = rw[3], d1 = rw[D + 3];
;             lg[0] += f0 * a0.x + f1 * b0.x + f2 * c0.x + f3 * d0.x; lg[1] += f0 * a0.y + f1 * b0.y + f2 * c0.y + f3 * d0.y;
;             lg[2] += f0 * a0.z + f1 * b0.z + f2 * c0.z + f3 * d0.z; lg[3] += f0 * a0.w + f1 * b0.w + f2 * c0.w + f3 * d0.w;
;             lg[4] += f0 * a1.x + f1 * b1.x + f2 * c1.x + f3 * d1.x; lg[5] += f0 * a1.y + f1 * b1.y + f2 * c1.y + f3 * d1.y;
;             lg[6] += f0 * a1.z + f1 * b1.z + f2 * c1.z + f3 * d1.z; lg[7] += f0 * a1.w + f1 * b1.w + f2 * c1.w + f3 * d1.w; }
; #pragma unroll
;         for (int e = 0; e < 8; ++e) lg[e] = wave_sum(lg[e]);
	v_mul_f32_e32 v24, v35, v24
	v_fmac_f32_e32 v24, v33, v20
	v_mul_f32_e32 v20, v35, v25
	v_fmac_f32_e32 v20, v33, v21
	s_waitcnt lgkmcnt(2)
	v_fmac_f32_e32 v20, v69, v29
	s_waitcnt lgkmcnt(1)
	v_fmac_f32_e32 v20, v7, v55
	v_fmac_f32_e32 v12, v33, v8
	v_mul_f32_e32 v8, v35, v13
	v_add_f32_e32 v62, v58, v20
	v_mul_f32_e32 v20, v35, v26
	v_fmac_f32_e32 v8, v33, v9
	v_fmac_f32_e32 v20, v33, v22
	v_fmac_f32_e32 v8, v69, v17
	v_fmac_f32_e32 v20, v69, v30
	s_waitcnt lgkmcnt(0)
	v_fmac_f32_e32 v8, v7, v65
	v_fmac_f32_e32 v20, v7, v56
	v_add_f32_e32 v58, v71, v8
	v_mul_f32_e32 v8, v35, v14
	v_add_f32_e32 v61, v59, v20
	v_mul_f32_e32 v20, v35, v27
	v_fmac_f32_e32 v8, v33, v10
	v_fmac_f32_e32 v20, v33, v23
	v_fmac_f32_e32 v8, v69, v18
	v_fmac_f32_e32 v20, v69, v31
	v_fmac_f32_e32 v8, v7, v66
	v_fmac_f32_e32 v20, v7, v57
	v_add_f32_e32 v57, v68, v8
	v_mul_f32_e32 v8, v35, v15
	v_fmac_f32_e32 v8, v33, v11
	v_fmac_f32_e32 v8, v69, v19
	v_fmac_f32_e32 v8, v7, v67
	v_add_f32_e32 v35, v32, v8
	v_fmac_f32_e32 v24, v69, v28
	v_fmac_f32_e32 v24, v7, v54
	v_add_f32_e32 v63, v53, v24
	v_fmac_f32_e32 v12, v69, v16
	v_fmac_f32_e32 v12, v7, v64
	v_add_f32_e32 v60, v60, v20
	v_add_f32_e32 v59, v70, v12
	v_mul_f32_e32 v55, v5, v136
	v_mul_f32_e32 v56, v4, v137
	v_mul_f32_e32 v53, v2, v139
	v_mov_b32_e32 v2, v1
	v_cvt_pk_fp8_f32 v2, v55, v56
	v_mul_f32_e32 v54, v3, v138
	v_cvt_pk_fp8_f32 v2, v54, v53 op_sel:[0,0,1]
	global_store_dword v[50:51], v2, off offset:768 sc0 sc1
	ds_read_b128 v[6:9], v37 offset:32768
	ds_read_b128 v[14:17], v37 offset:32784
	ds_read_b128 v[26:29], v37 offset:32800
	ds_read_b128 v[30:33], v37 offset:32816
	ds_read_b128 v[2:5], v52 offset:61440
	ds_read_b128 v[22:25], v52 offset:61456
	ds_read_b128 v[18:21], v52 offset:61472
	ds_read_b128 v[10:13], v52 offset:61488
	s_waitcnt lgkmcnt(6)
	v_mul_f32_e32 v14, v56, v14
	v_fmac_f32_e32 v14, v55, v6
	s_waitcnt lgkmcnt(5)
	v_fmac_f32_e32 v14, v54, v26
	s_waitcnt lgkmcnt(4)
	v_fmac_f32_e32 v14, v53, v30
	v_add_f32_e32 v6, v63, v14
	v_mul_f32_e32 v14, v56, v15
	v_fmac_f32_e32 v14, v55, v7
	v_fmac_f32_e32 v14, v54, v27
	v_fmac_f32_e32 v14, v53, v31
	v_add_f32_e32 v7, v62, v14
	v_mul_f32_e32 v14, v56, v16
	v_fmac_f32_e32 v14, v55, v8
	v_fmac_f32_e32 v14, v54, v28
	v_fmac_f32_e32 v14, v53, v32
	v_add_f32_e32 v8, v61, v14
	v_mul_f32_e32 v14, v56, v17
	v_fmac_f32_e32 v14, v55, v9
	v_fmac_f32_e32 v14, v54, v29
	v_fmac_f32_e32 v14, v53, v33
	v_add_f32_e32 v9, v60, v14
	s_waitcnt lgkmcnt(2)
	v_mul_f32_e32 v14, v56, v22
	v_fmac_f32_e32 v14, v55, v2
	v_mul_f32_e32 v2, v56, v23
	v_fmac_f32_e32 v2, v55, v3
	s_waitcnt lgkmcnt(1)
	v_fmac_f32_e32 v14, v54, v18
	v_fmac_f32_e32 v2, v54, v19
	s_waitcnt lgkmcnt(0)
	v_fmac_f32_e32 v14, v53, v10
	v_fmac_f32_e32 v2, v53, v11
	v_add_f32_e32 v10, v59, v14
	v_add_f32_e32 v14, v58, v2
	v_mul_f32_e32 v2, v56, v24
	v_fmac_f32_e32 v2, v55, v4
	v_fmac_f32_e32 v2, v54, v20
	v_fmac_f32_e32 v2, v53, v12
	v_add_f32_e32 v15, v57, v2
	v_mul_f32_e32 v2, v56, v25
	v_fmac_f32_e32 v2, v55, v5
	v_fmac_f32_e32 v2, v54, v21
	v_fmac_f32_e32 v2, v53, v13
	v_add_f32_e32 v16, v35, v2
	v_add_f32_dpp v10, v10, v10 quad_perm:[1,0,3,2] row_mask:0xf bank_mask:0xf bound_ctrl:1
	v_add_f32_dpp v2, v6, v6 quad_perm:[1,0,3,2] row_mask:0xf bank_mask:0xf bound_ctrl:1
	v_add_f32_dpp v6, v8, v8 quad_perm:[1,0,3,2] row_mask:0xf bank_mask:0xf bound_ctrl:1
	v_add_f32_dpp v8, v9, v9 quad_perm:[1,0,3,2] row_mask:0xf bank_mask:0xf bound_ctrl:1
	v_add_f32_dpp v2, v2, v2 quad_perm:[2,3,0,1] row_mask:0xf bank_mask:0xf bound_ctrl:1
	ds_swizzle_b32 v3, v2 offset:swizzle(SWAP,4)
	v_add_f32_dpp v12, v14, v14 quad_perm:[1,0,3,2] row_mask:0xf bank_mask:0xf bound_ctrl:1
	v_add_f32_dpp v14, v15, v15 quad_perm:[1,0,3,2] row_mask:0xf bank_mask:0xf bound_ctrl:1
	v_add_f32_dpp v16, v16, v16 quad_perm:[1,0,3,2] row_mask:0xf bank_mask:0xf bound_ctrl:1
	v_add_f32_dpp v6, v6, v6 quad_perm:[2,3,0,1] row_mask:0xf bank_mask:0xf bound_ctrl:1
	s_waitcnt lgkmcnt(0)
	v_add_f32_e32 v2, v2, v3
	ds_swizzle_b32 v3, v2 offset:swizzle(SWAP,8)
	v_add_f32_dpp v8, v8, v8 quad_perm:[2,3,0,1] row_mask:0xf bank_mask:0xf bound_ctrl:1
	v_add_f32_dpp v10, v10, v10 quad_perm:[2,3,0,1] row_mask:0xf bank_mask:0xf bound_ctrl:1
	v_add_f32_dpp v12, v12, v12 quad_perm:[2,3,0,1] row_mask:0xf bank_mask:0xf bound_ctrl:1
	v_add_f32_dpp v14, v14, v14 quad_perm:[2,3,0,1] row_mask:0xf bank_mask:0xf bound_ctrl:1
	s_waitcnt lgkmcnt(0)
	v_add_f32_e32 v2, v2, v3
	ds_swizzle_b32 v3, v2 offset:swizzle(SWAP,16)
	v_add_f32_dpp v16, v16, v16 quad_perm:[2,3,0,1] row_mask:0xf bank_mask:0xf bound_ctrl:1
	ds_swizzle_b32 v9, v8 offset:swizzle(SWAP,4)
	ds_swizzle_b32 v11, v10 offset:swizzle(SWAP,4)
	ds_swizzle_b32 v13, v12 offset:swizzle(SWAP,4)
	s_waitcnt lgkmcnt(3)
	v_add_f32_e32 v3, v2, v3
	v_add_f32_dpp v2, v7, v7 quad_perm:[1,0,3,2] row_mask:0xf bank_mask:0xf bound_ctrl:1
	ds_swizzle_b32 v7, v6 offset:swizzle(SWAP,4)
	ds_swizzle_b32 v15, v14 offset:swizzle(SWAP,4)
	v_add_f32_dpp v2, v2, v2 quad_perm:[2,3,0,1] row_mask:0xf bank_mask:0xf bound_ctrl:1
	ds_swizzle_b32 v4, v2 offset:swizzle(SWAP,4)
	ds_swizzle_b32 v17, v16 offset:swizzle(SWAP,4)
	s_waitcnt lgkmcnt(3)
	v_add_f32_e32 v6, v6, v7
	v_add_f32_e32 v8, v8, v9
	v_add_f32_e32 v10, v10, v11
	s_waitcnt lgkmcnt(1)
	v_add_f32_e32 v2, v2, v4
	v_add_f32_e32 v12, v12, v13
	v_add_f32_e32 v14, v14, v15
	s_waitcnt lgkmcnt(0)
; #define lane (lane_id())
; __device__ __forceinline__ void router_phase(const Ptrs& P, const float* gain, LAS unsigned char* lds, int vcu, int G, int tid, int wave, int lane) {
;     ...
;         for (int e = 0; e < 8; ++e) lg[e] = wave_sum(lg[e]);
;         int e0 = 0; float b0v = lg[0];
; #pragma unroll
;         for (int e = 1; e < 8; ++e) if (lg[e] > b0v) { b0v = lg[e]; e0 = e; }
;         int e1 = -1; float b1v = -__builtin_inff();
; #pragma unroll
;         for (int e = 0; e < 8; ++e) if (e != e0 && lg[e] > b1v) { b1v = lg[e]; e1 = e; }
;         const float g1 = 1.0f / (1.0f + __expf(b0v - b1v)), g0 = 1.0f - g1;
;         if (lane == 0) {
;             const unsigned k0 = __hip_atomic_fetch_add(lcnt + e0, 1u, __ATOMIC_RELAXED, __HIP_MEMORY_SCOPE_WORKGROUP);
;             const unsigned k1 = __hip_atomic_fetch_add(lcnt + e1, 1u, __ATOMIC_RELAXED, __HIP_MEMORY_SCOPE_WORKGROUP);
;             rinfo[li * 4 + 0] = (unsigned)e0 | ((unsigned)e1 << 8); rinfo[li * 4 + 1] = k0; rinfo[li * 4 + 2] = k1;
;             P.sel_g[2 * m] = g0; P.sel_g[2 * m + 1] = g1;
;         }
	v_add_f32_e32 v16, v16, v17
	ds_swizzle_b32 v4, v2 offset:swizzle(SWAP,8)
	ds_swizzle_b32 v7, v6 offset:swizzle(SWAP,8)
	ds_swizzle_b32 v9, v8 offset:swizzle(SWAP,8)
	ds_swizzle_b32 v11, v10 offset:swizzle(SWAP,8)
	ds_swizzle_b32 v13, v12 offset:swizzle(SWAP,8)
	ds_swizzle_b32 v15, v14 offset:swizzle(SWAP,8)
	ds_swizzle_b32 v17, v16 offset:swizzle(SWAP,8)
	s_waitcnt lgkmcnt(6)
	v_add_f32_e32 v2, v2, v4
	s_waitcnt lgkmcnt(5)
	v_add_f32_e32 v6, v6, v7
	s_waitcnt lgkmcnt(4)
	v_add_f32_e32 v8, v8, v9
	s_waitcnt lgkmcnt(3)
	v_add_f32_e32 v10, v10, v11
	s_waitcnt lgkmcnt(2)
	v_add_f32_e32 v12, v12, v13
	s_waitcnt lgkmcnt(1)
	v_add_f32_e32 v14, v14, v15
	s_waitcnt lgkmcnt(0)
	v_add_f32_e32 v16, v16, v17
	ds_swizzle_b32 v4, v2 offset:swizzle(SWAP,16)
	ds_swizzle_b32 v7, v6 offset:swizzle(SWAP,16)
	ds_swizzle_b32 v9, v8 offset:swizzle(SWAP,16)
	ds_swizzle_b32 v11, v10 offset:swizzle(SWAP,16)
	ds_swizzle_b32 v13, v12 offset:swizzle(SWAP,16)
	ds_swizzle_b32 v15, v14 offset:swizzle(SWAP,16)
	ds_swizzle_b32 v17, v16 offset:swizzle(SWAP,16)
	s_waitcnt lgkmcnt(6)
	v_add_f32_e32 v2, v2, v4
	s_waitcnt lgkmcnt(5)
	v_add_f32_e32 v6, v6, v7
	s_waitcnt lgkmcnt(4)
	v_add_f32_e32 v8, v8, v9
	s_waitcnt lgkmcnt(3)
	v_add_f32_e32 v10, v10, v11
	s_waitcnt lgkmcnt(2)
	v_add_f32_e32 v12, v12, v13
	s_waitcnt lgkmcnt(1)
	v_add_f32_e32 v14, v14, v15
	s_waitcnt lgkmcnt(0)
	v_add_f32_e32 v16, v16, v17
	v_mov_b32_e32 v5, v3
	v_mov_b32_e32 v4, v2
	v_mov_b32_e32 v7, v6
	v_mov_b32_e32 v9, v8
	v_mov_b32_e32 v11, v10
	v_mov_b32_e32 v13, v12
	v_mov_b32_e32 v15, v14
	v_mov_b32_e32 v17, v16
	v_permlane32_swap_b32_e32 v3, v5
	v_permlane32_swap_b32_e32 v2, v4
	v_permlane32_swap_b32_e32 v6, v7
	v_permlane32_swap_b32_e32 v8, v9
	v_permlane32_swap_b32_e32 v10, v11
	v_permlane32_swap_b32_e32 v12, v13
	v_permlane32_swap_b32_e32 v14, v15
	v_permlane32_swap_b32_e32 v16, v17
	s_and_saveexec_b64 s[28:29], s[38:39]
	s_cbranch_execz .LBB0_1474
	v_pk_add_f32 v[2:3], v[2:3], v[4:5]
	v_add_f32_e32 v6, v6, v7
	v_cmp_gt_f32_e32 vcc, v2, v3
	v_add_f32_e32 v8, v8, v9
	v_add_f32_e32 v10, v10, v11
	v_cndmask_b32_e32 v4, v3, v2, vcc
	v_cmp_gt_f32_e64 s[40:41], v6, v4
	v_add_f32_e32 v12, v12, v13
	v_cndmask_b32_e64 v5, 0, 1, vcc
	v_cndmask_b32_e64 v4, v4, v6, s[40:41]
	v_cmp_gt_f32_e64 s[42:43], v8, v4
	v_cndmask_b32_e64 v5, v5, 2, s[40:41]
	v_add_f32_e32 v14, v14, v15
	v_cndmask_b32_e64 v4, v4, v8, s[42:43]
	v_cmp_gt_f32_e64 s[44:45], v10, v4
	v_cndmask_b32_e64 v5, v5, 3, s[42:43]
	v_add_f32_e32 v16, v16, v17
	v_cndmask_b32_e64 v4, v4, v10, s[44:45]
	v_cmp_gt_f32_e64 s[46:47], v12, v4
	v_cndmask_b32_e64 v5, v5, 4, s[44:45]
	s_mov_b32 s27, 0xff800000
	v_cndmask_b32_e64 v4, v4, v12, s[46:47]
	v_cmp_gt_f32_e64 s[48:49], v14, v4
	v_cndmask_b32_e64 v5, v5, 5, s[46:47]
	v_cmp_nlg_f32_e64 s[52:53], s27, v3
	v_cndmask_b32_e64 v4, v4, v14, s[48:49]
	v_cndmask_b32_e64 v5, v5, 6, s[48:49]
	v_cmp_ngt_f32_e32 vcc, v16, v4
	s_and_b64 s[34:35], s[48:49], vcc
	s_ashr_i32 s27, s26, 31
	v_cndmask_b32_e32 v5, 7, v5, vcc
	v_cmp_eq_u32_e64 s[50:51], 0, v5
	s_or_b64 s[50:51], s[50:51], s[52:53]
	v_cmp_ne_u32_e64 s[48:49], 1, v5
	v_cndmask_b32_e64 v3, v3, v206, s[50:51]
	v_cmp_gt_f32_e64 s[52:53], v2, v3
	s_and_b64 s[48:49], s[48:49], s[52:53]
	v_cndmask_b32_e64 v2, v3, v2, s[48:49]
	v_cmp_ne_u32_e64 s[46:47], 2, v5
	v_cmp_gt_f32_e64 s[52:53], v6, v2
	s_and_b64 s[46:47], s[46:47], s[52:53]
	v_cndmask_b32_e64 v2, v2, v6, s[46:47]
	v_cmp_ne_u32_e64 s[44:45], 3, v5
	v_cmp_gt_f32_e64 s[52:53], v8, v2
	s_and_b64 s[44:45], s[44:45], s[52:53]
	v_cndmask_b32_e64 v2, v2, v8, s[44:45]
	v_cmp_ne_u32_e64 s[42:43], 4, v5
	v_cmp_gt_f32_e64 s[52:53], v10, v2
	s_and_b64 s[42:43], s[42:43], s[52:53]
	v_cndmask_b32_e64 v2, v2, v10, s[42:43]
	v_cmp_ne_u32_e64 s[40:41], 5, v5
	v_cmp_gt_f32_e64 s[52:53], v12, v2
	s_and_b64 s[40:41], s[40:41], s[52:53]
	v_cndmask_b32_e64 v2, v2, v12, s[40:41]
	v_cmp_ngt_f32_e64 s[52:53], v14, v2
	s_or_b64 s[52:53], s[34:35], s[52:53]
	v_cndmask_b32_e32 v4, v16, v4, vcc
	v_cndmask_b32_e64 v2, v14, v2, s[52:53]
	v_cmp_gt_f32_e64 s[54:55], v16, v2
	s_and_b64 s[54:55], vcc, s[54:55]
	v_cndmask_b32_e64 v3, 0, -1, s[50:51]
	v_cndmask_b32_e64 v2, v2, v16, s[54:55]
	v_sub_f32_e32 v2, v4, v2
	v_mul_f32_e32 v2, 0x3fb8aa3b, v2
	v_exp_f32_e32 v2, v2
	v_cndmask_b32_e64 v3, v3, 1, s[48:49]
	v_cndmask_b32_e64 v3, v3, 2, s[46:47]
	v_cndmask_b32_e64 v3, v3, 3, s[44:45]
	v_add_f32_e32 v2, 1.0, v2
	v_div_scale_f32 v4, s[34:35], v2, v2, 1.0
	v_rcp_f32_e32 v6, v4
	v_cndmask_b32_e64 v3, v3, 4, s[42:43]
	v_cndmask_b32_e64 v3, v3, 5, s[40:41]
	v_cndmask_b32_e64 v3, 6, v3, s[52:53]
	v_cndmask_b32_e64 v8, v3, 7, s[54:55]
	v_fma_f32 v3, -v4, v6, 1.0
	v_fmac_f32_e32 v6, v3, v6
	v_div_scale_f32 v3, vcc, 1.0, v2, 1.0
	v_mul_f32_e32 v7, v3, v6
	v_fma_f32 v9, -v4, v7, v3
	v_fmac_f32_e32 v7, v9, v6
	v_fma_f32 v3, -v4, v7, v3
	v_div_fmas_f32 v6, v3, v6, v7
	v_lshl_add_u32 v3, v5, 2, 0
	v_mov_b32_e32 v7, 1
	ds_add_rtn_u32 v3, v3, v7
	v_lshl_add_u32 v4, v8, 2, 0
	ds_add_rtn_u32 v4, v4, v7
	s_lshl_b64 s[34:35], s[26:27], 2
	v_readlane_b32 s44, v253, 44
	v_div_fixup_f32 v7, v6, v2, 1.0
	s_add_u32 s34, s18, s34
	v_readlane_b32 s53, v254, 43
	v_readlane_b32 s45, v253, 45
	v_readlane_b32 s50, v254, 40
	v_readlane_b32 s48, v254, 38
	v_sub_f32_e32 v6, 1.0, v7
	v_lshl_add_u32 v2, v8, 8, v5
	v_mov_b32_e32 v5, s23
	s_addc_u32 s35, s19, s35
	v_readlane_b32 s51, v254, 41
	v_readlane_b32 s49, v254, 39
	s_waitcnt lgkmcnt(0)
	ds_write_b96 v5, v[2:4]
	global_store_dwordx2 v1, v[6:7], s[34:35] sc0 sc1
	s_branch .LBB0_1474
